# MLA fast88 loop: static s_setprio 1 for waves 4-7 inside the tile loop (reset after), on top of read hoist + deferred P.V MFMA
# speedup vs baseline: 1.0103x; 1.0015x over previous
; #define ALAS __attribute__((address_space(3)))
; #define ATT_WAIT_BAR() asm volatile("s_waitcnt vmcnt(0) lgkmcnt(0)\n\ts_barrier" ::: "memory")
; #define MF_ISSUE_K(t, s) do { glds16(ksrc + (long)(t) * 64 * 512, (unsigned)__builtin_amdgcn_readfirstlane(kdst + (s) * KSLOT)); \
;         if (wid < 4) glds16(krsrc + (long)(t) * 64 * 32, (unsigned)__builtin_amdgcn_readfirstlane(krdst + (s) * KSLOT)); } while (0)
; __device__ __forceinline__ bool mla_unit_fast88(const Args& A, int b, int h, int qb, ALAS char* shm, const int tidb) {
;     ...
;     const int t_end = 4 * qb + 4;
;     const int cw = 4 * qb + (wid >> 1);
;     if (tid == 0) bailw[0] = 0;
;     MF_ISSUE_K(0, 0); MF_ISSUE_V(0, 0); MF_ISSUE_K(1, 1);
;     const unsigned char* Q8w = A.Q8 + (rowbase + q0 + wid * 32 + r32) * 768 + h * 96;
;     const unsigned char* Q8r = hi == 0 ? Q8w + 64 : A.ZERO;
;     v8i qf0, qf1;
;     { const u32x4 a0 = *(const u32x4*)(Q8w + 32 * hi), a1 = *(const u32x4*)(Q8w + 32 * hi + 16), b0 = *(const u32x4*)(Q8r), b1 = *(const u32x4*)(Q8r + 16);
;       qf0 = (v8i){(int)a0.x, (int)a0.y, (int)a0.z, (int)a0.w, (int)a1.x, (int)a1.y, (int)a1.z, (int)a1.w}; qf1 = (v8i){(int)b0.x, (int)b0.y, (int)b0.z, (int)b0.w, (int)b1.x, (int)b1.y, (int)b1.z, (int)b1.w}; }
;     const int sa8 = 0x7c7c7c7c, sb8 = 0x7b7b7b7b;
;     f32x16 o0 = {}, o1 = {}, ls = {};
;     const v8i ones8 = {0x38383838, 0x38383838, 0x38383838, 0x38383838, 0x38383838, 0x38383838, 0x38383838, 0x38383838};
;     const int vbo = ((lane >> 4) & 1) * 32 + (lane & 3) * 8 + (4 * hi + ((lane & 15) >> 2)) * 64;
;     ALAS const char* Kfr = shm + L_K + lane * 16;
;     ...
;     ATT_WAIT_BAR();
;     f32x16 cs[2][2];
;     { f32x16 z0 = {}, z1 = {}; ALAS const char* Ks_ = Kfr;
;       v8i k00, k01, k10, k11; M8_KFRAG(k00, Ks_, 0, 0); M8_KFRAG(k01, Ks_, 0, 1); M8_KFRAG(k10, Ks_, 1, 0); M8_KFRAG(k11, Ks_, 1, 1);
;       mfma8_acc(z0, k00, qf0, sa8, sb8); mfma8_acc(z1, k01, qf0, sa8, sb8); mfma8_acc(z0, k10, qf1, sa8, sb8); mfma8_acc(z1, k11, qf1, sa8, sb8);
;       asm volatile("s_nop 15\n\ts_nop 7" : "+v"(z0), "+v"(z1));
;       cs[0][0] = z0; cs[0][1] = z1; }
;     const float mhat = MF_ROWMAX(cs[0][0], cs[0][1]);
; #pragma unroll
;     for (int r = 0; r < 16; ++r) { cs[0][0][r] -= mhat; cs[0][1][r] -= mhat; }
;     f32x16 negm;
; #pragma unroll
;     for (int r = 0; r < 16; ++r) negm[r] = -mhat;
;     bool bailed = false; int ks = 0, vs = 0;
.LBB0_648:
	v_cmp_gt_u32_e32 vcc, 32, v154
	v_mov_b32_e32 v2, 0x800
	v_mov_b32_e32 v3, 0x8000
	v_cndmask_b32_e32 v2, 0, v2, vcc
	v_cndmask_b32_e64 v100, v2, v3, s[2:3]
	s_lshl_b32 s2, s6, 8
	v_mov_b32_e32 v101, v1
	s_lshl_b32 s37, s6, 2
	s_add_i32 s3, s45, 0x2000
	s_or_b32 s36, s30, s2
	s_lshl_b32 s2, s1, 5
	s_add_i32 s0, s37, 4
	s_add_i32 s47, s47, s37
	v_lshl_add_u64 v[2:3], v[146:147], 0, v[100:101]
	s_mov_b32 s4, m0
	s_mov_b32 m0, s3
	s_nop 0
	global_load_lds_dwordx4 v[2:3], off
	s_mov_b32 m0, s4
	s_ashr_i32 s3, s2, 31
	s_add_u32 s24, s36, s2
	v_or_b32_e32 v4, s24, v156
	v_mov_b64_e32 v[2:3], s[74:75]
	s_addc_u32 s25, s31, s3
	v_mad_u64_u32 v[2:3], s[2:3], v4, s67, v[2:3]
	v_mov_b32_e32 v4, 0x300
	v_mad_i32_i24 v3, s25, v4, v3
	v_lshl_add_u64 v[4:5], v[2:3], 0, 64
	v_mov_b32_e32 v6, s27
	v_cndmask_b32_e32 v5, v6, v5, vcc
	v_mov_b32_e32 v6, s26
	v_lshl_add_u64 v[2:3], v[2:3], 0, v[0:1]
	v_cndmask_b32_e32 v4, v6, v4, vcc
	global_load_dwordx4 v[134:137], v[2:3], off offset:16
	global_load_dwordx4 v[130:133], v[2:3], off
	global_load_dwordx4 v[142:145], v[4:5], off offset:16
	global_load_dwordx4 v[138:141], v[4:5], off
	v_lshlrev_b32_e32 v155, 4, v154
	s_mov_b32 s4, 0
	v_add_u32_e32 v157, 0, v155
	s_waitcnt vmcnt(0) lgkmcnt(0)
	s_barrier
	s_mov_b32 s18, s4
	s_mov_b32 s19, s4
	ds_read_b128 v[50:53], v157
	ds_read_b128 v[54:57], v157 offset:1024
	ds_read_b128 v[58:61], v157 offset:2048
	ds_read_b128 v[62:65], v157 offset:3072
	ds_read_b128 v[66:69], v157 offset:4096
	ds_read_b128 v[70:73], v157 offset:5120
	ds_read_b128 v[74:77], v157 offset:6144
	ds_read_b128 v[78:81], v157 offset:7168
	s_mov_b32 s5, s4
	s_mov_b32 s6, s4
	s_mov_b32 s7, s4
	s_mov_b32 s8, s4
	s_mov_b32 s9, s4
	s_mov_b32 s10, s4
	s_mov_b32 s11, s4
	s_mov_b32 s12, s4
	s_mov_b32 s13, s4
	s_mov_b32 s14, s4
	s_mov_b32 s15, s4
	s_mov_b32 s16, s4
	s_mov_b32 s17, s4
	v_mov_b64_e32 v[32:33], s[18:19]
	v_mov_b64_e32 v[30:31], s[16:17]
	v_mov_b64_e32 v[28:29], s[14:15]
	v_mov_b64_e32 v[26:27], s[12:13]
	v_mov_b64_e32 v[24:25], s[10:11]
	v_mov_b64_e32 v[22:23], s[8:9]
	v_mov_b64_e32 v[20:21], s[6:7]
	v_mov_b64_e32 v[18:19], s[4:5]
	v_mov_b64_e32 v[48:49], v[32:33]
	v_mov_b64_e32 v[46:47], v[30:31]
	v_mov_b64_e32 v[44:45], v[28:29]
	v_mov_b64_e32 v[42:43], v[26:27]
	v_mov_b64_e32 v[40:41], v[24:25]
	v_mov_b64_e32 v[38:39], v[22:23]
	v_mov_b64_e32 v[36:37], v[20:21]
	v_mov_b64_e32 v[34:35], v[18:19]
	v_mov_b32_e32 v16, v1
	v_mov_b32_e32 v17, v1
	v_mov_b32_e32 v2, v1
	v_mov_b32_e32 v3, v1
	v_mov_b32_e32 v4, v1
	v_mov_b32_e32 v5, v1
	v_mov_b32_e32 v6, v1
	v_mov_b32_e32 v7, v1
	v_mov_b32_e32 v8, v1
	v_mov_b32_e32 v9, v1
	v_mov_b32_e32 v10, v1
	v_mov_b32_e32 v11, v1
	v_mov_b32_e32 v12, v1
	v_mov_b32_e32 v13, v1
	v_mov_b32_e32 v14, v1
	v_mov_b32_e32 v15, v1
	s_mov_b32 s41, s31
	s_mov_b32 s5, 3
	v_mul_hi_u32_u24_e32 v149, 3, v100
	v_mul_u32_u24_e32 v148, 3, v100
	v_lshl_add_u64 v[150:151], v[98:99], 0, s[78:79]
	s_waitcnt vmcnt(0) lgkmcnt(0)
	v_mfma_scale_f32_32x32x64_f8f6f4 v[34:49], v[50:57], v[130:137], v[34:49], v247, v253 op_sel_hi:[0,0,0]
	s_waitcnt lgkmcnt(4)
	v_mfma_scale_f32_32x32x64_f8f6f4 v[18:33], v[58:65], v[130:137], v[18:33], v247, v253 op_sel_hi:[0,0,0]
	s_waitcnt vmcnt(0) lgkmcnt(2)
	v_mfma_scale_f32_32x32x64_f8f6f4 v[34:49], v[66:73], v[138:145], v[34:49], v247, v253 op_sel_hi:[0,0,0]
	s_waitcnt lgkmcnt(0)
	v_mfma_scale_f32_32x32x64_f8f6f4 v[18:33], v[74:81], v[138:145], v[18:33], v247, v253 op_sel_hi:[0,0,0]
	s_nop 0
	s_nop 15
	s_nop 7
	s_nop 0
	v_max3_f32 v0, v34, v18, v38
	s_nop 0
	v_max3_f32 v0, v0, v22, v42
	s_nop 0
	v_max3_f32 v0, v0, v26, v46
	s_nop 0
	v_max_f32_e32 v0, v0, v30
	v_max3_f32 v50, v35, v19, v39
	s_nop 0
	v_max3_f32 v50, v50, v23, v43
	s_nop 0
	v_max3_f32 v50, v50, v27, v47
	s_nop 0
	v_max_f32_e32 v50, v50, v31
	v_max3_f32 v51, v36, v20, v40
	s_nop 0
	v_max3_f32 v51, v51, v24, v44
	s_nop 0
	v_max3_f32 v51, v51, v28, v48
	s_nop 0
	v_max_f32_e32 v51, v51, v32
	v_max3_f32 v52, v37, v21, v41
	s_nop 0
	v_max3_f32 v52, v52, v25, v45
	s_nop 0
	v_max3_f32 v52, v52, v29, v49
	s_nop 0
	v_max_f32_e32 v52, v52, v33
	v_max3_f32 v0, v0, v50, v51
	s_nop 0
	v_max_f32_e32 v0, v0, v52
	s_nop 0
	v_mov_b32_e32 v50, v0
	s_nop 1
	v_permlane32_swap_b32_e32 v0, v50
	v_max_f32_e32 v50, v50, v50
	v_max_f32_e32 v0, v0, v0
	v_max_f32_e32 v0, v0, v50
	v_sub_f32_e32 v65, v49, v0
	v_sub_f32_e32 v64, v48, v0
	v_sub_f32_e32 v63, v47, v0
	v_sub_f32_e32 v62, v46, v0
	v_sub_f32_e32 v61, v45, v0
	v_sub_f32_e32 v60, v44, v0
	v_sub_f32_e32 v59, v43, v0
	v_sub_f32_e32 v58, v42, v0
	v_sub_f32_e32 v57, v41, v0
	v_sub_f32_e32 v56, v40, v0
	v_sub_f32_e32 v55, v39, v0
	v_sub_f32_e32 v54, v38, v0
	v_sub_f32_e32 v53, v37, v0
	v_sub_f32_e32 v52, v36, v0
	v_sub_f32_e32 v51, v35, v0
	v_sub_f32_e32 v50, v34, v0
	v_sub_f32_e32 v97, v33, v0
	v_sub_f32_e32 v96, v32, v0
	v_sub_f32_e32 v95, v31, v0
	v_sub_f32_e32 v94, v30, v0
	v_sub_f32_e32 v93, v29, v0
	v_sub_f32_e32 v92, v28, v0
	v_sub_f32_e32 v91, v27, v0
	v_sub_f32_e32 v90, v26, v0
	v_sub_f32_e32 v89, v25, v0
	v_sub_f32_e32 v88, v24, v0
	v_sub_f32_e32 v87, v23, v0
	v_sub_f32_e32 v86, v22, v0
	v_sub_f32_e32 v85, v21, v0
	v_sub_f32_e32 v84, v20, v0
	v_sub_f32_e32 v83, v19, v0
	v_sub_f32_e32 v82, v18, v0
	v_xor_b32_e32 v66, 0x80000000, v0
	v_mov_b64_e32 v[32:33], v[16:17]
	v_mov_b64_e32 v[48:49], v[16:17]
	v_mov_b32_e32 v67, v66
	v_mov_b32_e32 v68, v66
	v_mov_b32_e32 v69, v66
	v_mov_b32_e32 v70, v66
	v_mov_b32_e32 v71, v66
	v_mov_b32_e32 v72, v66
	v_mov_b32_e32 v73, v66
	v_mov_b32_e32 v74, v66
	v_mov_b32_e32 v75, v66
	v_mov_b32_e32 v76, v66
	v_mov_b32_e32 v77, v66
	v_mov_b32_e32 v78, v66
	v_mov_b32_e32 v79, v66
	v_mov_b32_e32 v80, v66
	v_mov_b32_e32 v81, v66
	v_lshlrev_b32_e32 v0, 1, v100
	v_mov_b64_e32 v[30:31], v[14:15]
	v_mov_b64_e32 v[28:29], v[12:13]
	v_mov_b64_e32 v[26:27], v[10:11]
	v_mov_b64_e32 v[24:25], v[8:9]
	v_mov_b64_e32 v[22:23], v[6:7]
	v_mov_b64_e32 v[20:21], v[4:5]
	v_mov_b64_e32 v[18:19], v[2:3]
	v_mov_b64_e32 v[46:47], v[14:15]
	v_mov_b64_e32 v[44:45], v[12:13]
	v_mov_b64_e32 v[42:43], v[10:11]
	v_mov_b64_e32 v[40:41], v[8:9]
	v_mov_b64_e32 v[38:39], v[6:7]
	v_mov_b64_e32 v[36:37], v[4:5]
	v_mov_b64_e32 v[34:35], v[2:3]
	v_mov_b32_e32 v172, 0
	v_mov_b32_e32 v173, 0
	v_mov_b32_e32 v174, 0
	v_mov_b32_e32 v175, 0
	v_mov_b32_e32 v176, 0
	v_mov_b32_e32 v177, 0
	v_mov_b32_e32 v178, 0
	v_mov_b32_e32 v179, 0
	v_mov_b32_e32 v180, 0
	v_mov_b32_e32 v181, 0
	v_mov_b32_e32 v182, 0
	v_mov_b32_e32 v183, 0
	v_mov_b32_e32 v184, 0
	v_mov_b32_e32 v185, 0
	v_mov_b32_e32 v186, 0
	v_mov_b32_e32 v187, 0
	v_readlane_b32 s2, v254, 1
	s_nop 3
	s_cmp_lt_u32 s2, 4
	s_cbranch_scc1 .Lmla_prio_skip
	s_setprio 1
; #define ALAS __attribute__((address_space(3)))
; #define MF_ISSUE_K(t, s) do { glds16(ksrc + (long)(t) * 64 * 512, (unsigned)__builtin_amdgcn_readfirstlane(kdst + (s) * KSLOT)); \
;         if (wid < 4) glds16(krsrc + (long)(t) * 64 * 32, (unsigned)__builtin_amdgcn_readfirstlane(krdst + (s) * KSLOT)); } while (0)
; #define MF_ISSUE_V(t, s) glds16(vsrc + (long)(t) * 64 * 512, (unsigned)__builtin_amdgcn_readfirstlane(vdst + (s) * VSLOT))
; #define MF_ISSUE_K(t, s) glds16(ks8 + (long)(t) * kst8, (unsigned)__builtin_amdgcn_readfirstlane(kdst + (s) * KSLOT))
; #define MF_ISSUE_V(t, s) glds16(vsrc + (long)(t) * 64 * 512, (unsigned)__builtin_amdgcn_readfirstlane(vdst + (s) * VSLOT))
; #define M8_KFRAG(dst, base, m, kh) do { const u32x4 lo_ = *(ALAS const u32x4*)((base) + (((m) * 2 + (kh)) * 2) * 1024), hi_ = *(ALAS const u32x4*)((base) + (((m) * 2 + (kh)) * 2 + 1) * 1024); \
;         dst = (v8i){(int)lo_.x, (int)lo_.y, (int)lo_.z, (int)lo_.w, (int)hi_.x, (int)hi_.y, (int)hi_.z, (int)hi_.w}; } while (0)
; #define MF_ISSUE_K(t, s) glds16(ks8 + (long)(t) * kst8, (unsigned)__builtin_amdgcn_readfirstlane(kdst + (s) * KSLOT))
; #define MF_ISSUE_V(t, s) do { if (wid < 4) glds16(vs8 + (long)(t) * 4096, (unsigned)__builtin_amdgcn_readfirstlane(vdst + (s) * 4096)); } while (0)
; #define M8_KFRAG(dst, base, m, kh) do { const u32x4 lo_ = *(ALAS const u32x4*)((base) + (((m) * 2 + (kh)) * 2) * 1024), hi_ = *(ALAS const u32x4*)((base) + (((m) * 2 + (kh)) * 2 + 1) * 1024); \
;         dst = (v8i){(int)lo_.x, (int)lo_.y, (int)lo_.z, (int)lo_.w, (int)hi_.x, (int)hi_.y, (int)hi_.z, (int)hi_.w}; } while (0)
; __device__ __forceinline__ bool mla_unit_fast88(const Args& A, int b, int h, int qb, ALAS char* shm, const int tidb) {
;     ...
;         for (int p = 0; p < 2; ++p) {
;             const int t = t2 + p; f32x16 &C0 = cs[p][0], &C1 = cs[p][1], &N0 = cs[p ^ 1][0], &N1 = cs[p ^ 1][1];
;             const bool vis = !bailed && t <= cw;
;             const int ks1 = ks == 2 ? 0 : ks + 1, ks2 = ks1 == 2 ? 0 : ks1 + 1;
;             if (t + 2 < t_end) MF_ISSUE_K(t + 2, ks2);
;             if (t + 1 < t_end) MF_ISSUE_V(t + 1, vs ^ 1);
;             if (vis) {
;                 {
;                     ALAS const char* Ks_ = Kfr + ks1 * KSLOT;
;                     v8i kfa, kfb; M8_KFRAG(kfa, Ks_, 0, 0);
;                     M8_KFRAG(kfb, Ks_, 0, 1);
.Lmla_prio_skip:
.LBB0_649:
	s_add_i32 s2, s4, 1
	s_cmp_lg_u32 s4, 2
	s_cselect_b32 s4, s2, 0
	v_lshl_add_u32 v171, s4, 13, v157
	ds_read_b128 v[114:117], v171
	ds_read_b128 v[118:121], v171 offset:1024
	ds_read_b128 v[164:167], v171 offset:2048
	ds_read_b128 v[168:171], v171 offset:3072
	v_mfma_scale_f32_32x32x64_f8f6f4 v[18:33], v[180:187], v[172:179], v[18:33], v251, v247 op_sel_hi:[0,0,0] cbsz:1
	s_add_i32 s6, s5, -1
	s_cmp_lt_u32 s6, s0
	s_cselect_b64 s[2:3], -1, 0
	s_and_b64 vcc, exec, s[2:3]
	v_lshl_add_u64 v[152:153], v[146:147], 0, v[0:1]
	s_cbranch_vccz .LBB0_651
	s_lshl_b32 s7, s4, 13
	s_addk_i32 s7, 0x2000
	s_cmp_lg_u32 s4, 2
	s_cselect_b32 s7, s7, 0
	v_lshl_add_u64 v[158:159], v[146:147], 0, v[0:1]
	s_add_i32 s7, s7, s45
	s_mov_b32 s8, m0
	s_mov_b32 m0, s7
	s_nop 0
	global_load_lds_dwordx4 v[158:159], off
	s_mov_b32 m0, s8

; __device__ __forceinline__ int crow(int r, int hi) { return (r & 3) + 8 * (r >> 2) + 4 * hi; }
; #define ATT_WAIT_BAR() asm volatile("s_waitcnt vmcnt(0) lgkmcnt(0)\n\ts_barrier" ::: "memory")
; __device__ __forceinline__ bool mla_unit_fast88(const Args& A, int b, int h, int qb, ALAS char* shm, const int tidb) {
;     ...
;                 mfma8p_acc(o1, pf, vf1, 0x7f7f7f7f, 0x7c7c7c7c);
;                 mfma8p_acc(ls, pf, ones8, 0x7f7f7f7f, 0x7f7f7f7f);
;                 __builtin_amdgcn_sched_barrier(0);
;             }
;             ks = ks1; vs ^= 1;
;             ATT_WAIT_BAR();
;         }
;     }
;     asm volatile("s_nop 15\n\ts_nop 15" : "+v"(o0), "+v"(o1), "+v"(ls));
;     { bool bad_ = false;
; #pragma unroll
;       for (int r = 0; r < 16; ++r) bad_ |= !(ls[r] > 1.0e-30f && ls[r] < 5.7e4f);
;       if (__any(bad_)) bailed = true; }
;     if (bailed && lane == 0) bailw[0] = 1;
;     if (r32 == 0) {
; #pragma unroll
;         for (int r = 0; r < 16; ++r) wsf[32 + crow(r, hi)] = ls[r]; }
.LBB0_665:
	s_setprio 0
	v_mfma_scale_f32_32x32x64_f8f6f4 v[18:33], v[180:187], v[172:179], v[18:33], v251, v247 op_sel_hi:[0,0,0] cbsz:1
	s_mov_b32 s6, 0x475ea800
	s_nop 15
	s_nop 15
	s_nop 0
	v_cmp_nlt_f32_e32 vcc, s39, v34
	v_cmp_ngt_f32_e64 s[2:3], s6, v34
	s_or_b64 s[4:5], vcc, s[2:3]
	v_cmp_nlt_f32_e32 vcc, s39, v35
	v_cmp_ngt_f32_e64 s[2:3], s6, v35
	s_or_b64 s[2:3], vcc, s[2:3]
	s_or_b64 s[4:5], s[4:5], s[2:3]
	v_cmp_nlt_f32_e32 vcc, s39, v36
	v_cmp_ngt_f32_e64 s[2:3], s6, v36
	s_or_b64 s[2:3], vcc, s[2:3]
	s_or_b64 s[4:5], s[2:3], s[4:5]
	v_cmp_nlt_f32_e32 vcc, s39, v37
	v_cmp_ngt_f32_e64 s[2:3], s6, v37
	s_or_b64 s[2:3], vcc, s[2:3]
	s_or_b64 s[4:5], s[2:3], s[4:5]
	v_cmp_nlt_f32_e32 vcc, s39, v38
	v_cmp_ngt_f32_e64 s[2:3], s6, v38
	s_or_b64 s[2:3], vcc, s[2:3]
	s_or_b64 s[4:5], s[2:3], s[4:5]
	v_cmp_nlt_f32_e32 vcc, s39, v39
	v_cmp_ngt_f32_e64 s[2:3], s6, v39
	s_or_b64 s[2:3], vcc, s[2:3]
	s_or_b64 s[4:5], s[2:3], s[4:5]
	v_cmp_nlt_f32_e32 vcc, s39, v40
	v_cmp_ngt_f32_e64 s[2:3], s6, v40
	s_or_b64 s[2:3], vcc, s[2:3]
	s_or_b64 s[4:5], s[2:3], s[4:5]
	v_cmp_nlt_f32_e32 vcc, s39, v41
	v_cmp_ngt_f32_e64 s[2:3], s6, v41
	s_or_b64 s[2:3], vcc, s[2:3]
	s_or_b64 s[4:5], s[2:3], s[4:5]
	v_cmp_nlt_f32_e32 vcc, s39, v42
	v_cmp_ngt_f32_e64 s[2:3], s6, v42
	s_or_b64 s[2:3], vcc, s[2:3]
	s_or_b64 s[4:5], s[2:3], s[4:5]
	v_cmp_nlt_f32_e32 vcc, s39, v43
	v_cmp_ngt_f32_e64 s[2:3], s6, v43
	s_or_b64 s[2:3], vcc, s[2:3]
	s_or_b64 s[4:5], s[2:3], s[4:5]
	v_cmp_nlt_f32_e32 vcc, s39, v44
	v_cmp_ngt_f32_e64 s[2:3], s6, v44
	s_or_b64 s[2:3], vcc, s[2:3]
	s_or_b64 s[4:5], s[2:3], s[4:5]
	v_cmp_nlt_f32_e32 vcc, s39, v45
	v_cmp_ngt_f32_e64 s[2:3], s6, v45
	s_or_b64 s[2:3], vcc, s[2:3]
	s_or_b64 s[4:5], s[2:3], s[4:5]
	v_cmp_nlt_f32_e32 vcc, s39, v46
	v_cmp_ngt_f32_e64 s[2:3], s6, v46
	s_or_b64 s[2:3], vcc, s[2:3]
	s_or_b64 s[4:5], s[2:3], s[4:5]
	v_cmp_nlt_f32_e32 vcc, s39, v47
	v_cmp_ngt_f32_e64 s[2:3], s6, v47
	s_or_b64 s[2:3], vcc, s[2:3]
	s_or_b64 s[4:5], s[2:3], s[4:5]
	v_cmp_nlt_f32_e32 vcc, s39, v48
	v_cmp_ngt_f32_e64 s[2:3], s6, v48
	s_or_b64 s[2:3], vcc, s[2:3]
	s_or_b64 s[4:5], s[2:3], s[4:5]
	v_cmp_nlt_f32_e32 vcc, s39, v49
	v_cmp_ngt_f32_e64 s[2:3], s6, v49
	s_or_b64 s[2:3], vcc, s[2:3]
	s_or_b64 s[2:3], s[2:3], s[4:5]
	v_cndmask_b32_e64 v0, 0, 1, s[2:3]
	v_cmp_ne_u32_e32 vcc, 0, v0
	s_cmp_lg_u64 vcc, 0
	s_cselect_b64 s[2:3], -1, 0
	v_cmp_eq_u32_e32 vcc, 0, v154
	s_and_b64 s[4:5], s[2:3], vcc
	s_and_saveexec_b64 s[2:3], s[4:5]
	v_mov_b32_e32 v0, s38
	ds_write_b32 v0, v252
	s_or_b64 exec, exec, s[2:3]
	s_and_b32 s2, s43, 0x3fffffc0
	s_lshl_b32 s2, s2, 2
	v_lshrrev_b32_e32 v51, 5, v154
	s_add_i32 s2, s2, 0
	v_cmp_eq_u32_e32 vcc, 0, v156
	v_lshl_add_u32 v50, v51, 4, s2
	s_and_saveexec_b64 s[2:3], vcc
	s_cbranch_execz .LBB0_669
	ds_write_b128 v50, v[34:37] offset:53376
	ds_write_b128 v50, v[38:41] offset:53408
	ds_write_b128 v50, v[42:45] offset:53440
	ds_write_b128 v50, v[46:49] offset:53472
